# expected-empty gathered MoBA tickets merged per list (one flagged ticket walks the remaining chunks): 560 fewer tickets per attention phase
# baseline (speedup 1.0000x reference)
; __device__ __forceinline__ void attn_conv_phase(const Ptrs& P, const att::AttnArgs& A, int layer, unsigned* qctr, unsigned char* lds, const int wave_) {
;     ...
;     for (;;) {
;         __syncthreads();
;         if (t0_) TK[0] = nxt_;
;         __syncthreads();
;         const int tk = __builtin_amdgcn_readfirstlane(TK[0]);
;         if (tk >= att::N_TICKETS) break;
;         if (t0_) nxt_ = (int)__hip_atomic_fetch_add(qctr, 1u, __ATOMIC_RELAXED, __HIP_MEMORY_SCOPE_AGENT);
.Lticket_top_nowait:
	s_barrier
	s_and_saveexec_b64 s[0:1], s[88:89]
	v_mov_b32_e32 v0, s71
	ds_write_b32 v0, v133
	s_or_b64 exec, exec, s[0:1]
	v_mov_b32_e32 v0, s71
	s_waitcnt lgkmcnt(0)
	s_barrier
	ds_read_b32 v0, v0
	s_mov_b64 s[14:15], -1
	s_waitcnt lgkmcnt(0)
	v_readfirstlane_b32 s0, v0
	s_cmpk_gt_i32 s0, 0xed5
	s_cbranch_scc1 .LBB0_439
	s_and_saveexec_b64 s[14:15], s[88:89]
	s_cbranch_execz .LBB0_447
	s_mov_b64 s[22:23], exec
	v_mbcnt_lo_u32_b32 v0, s22, 0
	v_mbcnt_hi_u32_b32 v0, s23, v0
	v_cmp_eq_u32_e32 vcc, 0, v0
	s_and_saveexec_b64 s[18:19], vcc
	s_cbranch_execz .LBB0_446
	s_bcnt1_i32_b64 s1, s[22:23]
	v_mov_b32_e32 v2, s1
	global_atomic_add v133, v1, v2, s[86:87] sc0

; __device__ __forceinline__ unsigned ld_sc1(const unsigned* p) { return __hip_atomic_load(p, __ATOMIC_RELAXED, __HIP_MEMORY_SCOPE_AGENT); }
; template <int mode> __device__ __forceinline__ void attn_unit(const AttnArgs& A, const int b, const int h, const int sub, char* shm, const int wave_) {
;     ...
;     if (mode == 3) { gk = sub >> 4; const int c = sub & 15; const int li = (b * 5 + (h - 6)) * 15 + gk;
;         gcnt = __builtin_amdgcn_readfirstlane((int)ld_sc1(A.mcnt + li));
;         if (c * 256 >= gcnt) return;
; __device__ __forceinline__ void attn_conv_phase(const Ptrs& P, const att::AttnArgs& A, int layer, unsigned* qctr, unsigned char* lds, const int wave_) {
;     ...
;         } else if (code & 0x4000) {
;             if (!selrdy) { if (t0_) { unsigned spins = 0; while (att::ld_sc1(A.mdone) < (unsigned)att::N_SEL && ++spins < (1u << 24)) __builtin_amdgcn_s_sleep(8); } selrdy = true; __syncthreads(); }
;             att::attn_unit<3>(A, (code >> 11) & 1, 6 + ((code >> 8) & 7), code & 0xff, shm, wave_);
.LBB0_665:
	s_or_b64 exec, exec, s[0:1]
	s_bitcmp1_b32 s26, 12
	s_cbranch_scc0 .LBB0_666
	s_bfe_u32 s0, s26, 0x40004
	s_and_b32 s1, s26, 15
	s_add_i32 s0, s0, s1
	s_cmp_ge_u32 s0, 14
	s_cbranch_scc1 .LBB0_666
	s_add_i32 s26, s26, 1
	s_waitcnt vmcnt(0) lgkmcnt(0)
	s_barrier
	s_branch .LBB0_516

_ZN3attL9ATT_ORDERE:
	.short	8207
	.short	8206
	.short	8205
	.short	8204
	.short	8203
	.short	8202
	.short	8201
	.short	8200
	.short	8199
	.short	8198
	.short	8197
	.short	8196
	.short	8195
	.short	8194
	.short	8193
	.short	8271
	.short	8270
	.short	8269
	.short	8268
	.short	8267
	.short	8266
	.short	8265
	.short	8264
	.short	8263
	.short	8262
	.short	8261
	.short	8260
	.short	8259
	.short	8258
	.short	8257
	.short	8335
	.short	8334
	.short	8333
	.short	8332
	.short	8331
	.short	8330
	.short	8329
	.short	8328
	.short	8327
	.short	8326
	.short	8325
	.short	8324
	.short	8323
	.short	8322
	.short	8321
	.short	8399
	.short	8398
	.short	8397
	.short	8396
	.short	8395
	.short	8394
	.short	8393
	.short	8392
	.short	8391
	.short	8390
	.short	8389
	.short	8388
	.short	8387
	.short	8386
	.short	8385
	.short	8463
	.short	8462
	.short	8461
	.short	8460
	.short	8459
	.short	8458
	.short	8457
	.short	8456
	.short	8455
	.short	8454
	.short	8453
	.short	8452
	.short	8451
	.short	8450
	.short	8449
	.short	8719
	.short	8718
	.short	8717
	.short	8716
	.short	8715
	.short	8714
	.short	8713
	.short	8712
	.short	8711
	.short	8710
	.short	8709
	.short	8708
	.short	8707
	.short	8706
	.short	8705
	.short	8783
	.short	8782
	.short	8781
	.short	8780
	.short	8779
	.short	8778
	.short	8777
	.short	8776
	.short	8775
	.short	8774
	.short	8773
	.short	8772
	.short	8771
	.short	8770
	.short	8769
	.short	8847
	.short	8846
	.short	8845
	.short	8844
	.short	8843
	.short	8842
	.short	8841
	.short	8840
	.short	8839
	.short	8838
	.short	8837
	.short	8836
	.short	8835
	.short	8834
	.short	8833
	.short	8911
	.short	8910
	.short	8909
	.short	8908
	.short	8907
	.short	8906
	.short	8905
	.short	8904
	.short	8903
	.short	8902
	.short	8901
	.short	8900
	.short	8899
	.short	8898
	.short	8897
	.short	8975
	.short	8974
	.short	8973
	.short	8972
	.short	8971
	.short	8970
	.short	8969
	.short	8968
	.short	8967
	.short	8966
	.short	8965
	.short	8964
	.short	8963
	.short	8962
	.short	8961
	.short	2063
	.short	32768
	.short	32769
	.short	2127
	.short	32770
	.short	32771
	.short	2191
	.short	32772
	.short	32773
	.short	2255
	.short	32774
	.short	32775
	.short	2319
	.short	32776
	.short	32777
	.short	2575
	.short	32778
	.short	32779
	.short	2639
	.short	32780
	.short	32781
	.short	32782
	.short	2703
	.short	32783
	.short	32784
	.short	2767
	.short	32785
	.short	32786
	.short	2831
	.short	32787
	.short	32788
	.short	2062
	.short	32789
	.short	32790
	.short	2126
	.short	32791
	.short	32792
	.short	2190
	.short	32793
	.short	32794
	.short	2254
	.short	32795
	.short	32796
	.short	32797
	.short	2318
	.short	32798
	.short	32799
	.short	2574
	.short	32800
	.short	32801
	.short	2638
	.short	32802
	.short	32803
	.short	2702
	.short	32804
	.short	32805
	.short	2766
	.short	32806
	.short	32807
	.short	2830
	.short	32808
	.short	32809
	.short	32810
	.short	2061
	.short	32811
	.short	32812
	.short	2125
	.short	32813
	.short	32814
	.short	2189
	.short	32815
	.short	32816
	.short	2253
	.short	32817
	.short	32818
	.short	2317
	.short	32819
	.short	32820
	.short	2573
	.short	32821
	.short	32822
	.short	2637
	.short	32823
	.short	32824
	.short	32825
	.short	2701
	.short	32826
	.short	32827
	.short	2765
	.short	32828
	.short	32829
	.short	2829
	.short	32830
	.short	32831
	.short	2060
	.short	32832
	.short	32833
	.short	2124
	.short	32834
	.short	32835
	.short	2188
	.short	32836
	.short	32837
	.short	32838
	.short	2252
	.short	32839
	.short	32840
	.short	2316
	.short	32841
	.short	32842
	.short	2572
	.short	32843
	.short	32844
	.short	2636
	.short	32845
	.short	32846
	.short	2700
	.short	32847
	.short	32848
	.short	2764
	.short	32849
	.short	32850
	.short	2828
	.short	32851
	.short	32852
	.short	32853
	.short	2059
	.short	32854
	.short	32855
	.short	2123
	.short	32856
	.short	32857
	.short	2187
	.short	32858
	.short	32859
	.short	2251
	.short	32860
	.short	32861
	.short	2315
	.short	32862
	.short	32863
	.short	2571
	.short	32864
	.short	32865
	.short	32866
	.short	2635
	.short	32867
	.short	32868
	.short	2699
	.short	32869
	.short	32870
	.short	2763
	.short	32871
	.short	32872
	.short	2827
	.short	32873
	.short	32874
	.short	2058
	.short	32875
	.short	32876
	.short	2122
	.short	32877
	.short	32878
	.short	2186
	.short	32879
	.short	32880
	.short	32881
	.short	2250
	.short	32882
	.short	32883
	.short	2314
	.short	32884
	.short	32885
	.short	2570
	.short	32886
	.short	32887
	.short	2634
	.short	32888
	.short	32889
	.short	2698
	.short	32890
	.short	32891
	.short	2762
	.short	32892
	.short	32893
	.short	32894
	.short	2826
	.short	32895
	.short	32896
	.short	2057
	.short	32897
	.short	32898
	.short	2121
	.short	32899
	.short	32900
	.short	2185
	.short	32901
	.short	32902
	.short	2249
	.short	32903
	.short	32904
	.short	2313
	.short	32905
	.short	32906
	.short	2569
	.short	32907
	.short	32908
	.short	32909
	.short	2633
	.short	32910
	.short	32911
	.short	2697
	.short	32912
	.short	32913
	.short	2761
	.short	32914
	.short	32915
	.short	2825
	.short	32916
	.short	32917
	.short	2056
	.short	32918
	.short	32919
	.short	2120
	.short	32920
	.short	32921
	.short	32922
	.short	2184
	.short	32923
	.short	32924
	.short	2248
	.short	32925
	.short	32926
	.short	2312
	.short	32927
	.short	32928
	.short	2568
	.short	32929
	.short	32930
	.short	2632
	.short	32931
	.short	32932
	.short	2696
	.short	32933
	.short	32934
	.short	2760
	.short	32935
	.short	32936
	.short	32937
	.short	2824
	.short	32938
	.short	32939
	.short	2055
	.short	32940
	.short	32941
	.short	2119
	.short	32942
	.short	32943
	.short	2183
	.short	32944
	.short	32945
	.short	2247
	.short	32946
	.short	32947
	.short	2311
	.short	32948
	.short	32949
	.short	32950
	.short	2567
	.short	32951
	.short	32952
	.short	2631
	.short	32953
	.short	32954
	.short	2695
	.short	32955
	.short	32956
	.short	2759
	.short	32957
	.short	32958
	.short	2823
	.short	32959
	.short	32960
	.short	2054
	.short	32961
	.short	32962
	.short	2118
	.short	32963
	.short	32964
	.short	32965
	.short	2182
	.short	32966
	.short	32967
	.short	2246
	.short	32968
	.short	32969
	.short	2310
	.short	32970
	.short	32971
	.short	2566
	.short	32972
	.short	32973
	.short	2630
	.short	32974
	.short	32975
	.short	2694
	.short	32976
	.short	32977
	.short	32978
	.short	2758
	.short	32979
	.short	32980
	.short	2822
	.short	32981
	.short	32982
	.short	2053
	.short	32983
	.short	32984
	.short	2117
	.short	32985
	.short	32986
	.short	2181
	.short	32987
	.short	32988
	.short	2245
	.short	32989
	.short	32990
	.short	2309
	.short	32991
	.short	32992
	.short	32993
	.short	2565
	.short	32994
	.short	32995
	.short	2629
	.short	32996
	.short	32997
	.short	2693
	.short	32998
	.short	32999
	.short	2757
	.short	33000
	.short	33001
	.short	2821
	.short	33002
	.short	33003
	.short	2052
	.short	33004
	.short	33005
	.short	33006
	.short	2116
	.short	33007
	.short	33008
	.short	2180
	.short	33009
	.short	33010
	.short	2244
	.short	33011
	.short	33012
	.short	2308
	.short	33013
	.short	33014
	.short	2564
	.short	33015
	.short	33016
	.short	2628
	.short	33017
	.short	33018
	.short	2692
	.short	33019
	.short	33020
	.short	33021
	.short	2756
	.short	33022
	.short	33023
	.short	2820
	.short	33024
	.short	33025
	.short	2051
	.short	33026
	.short	33027
	.short	2115
	.short	33028
	.short	33029
	.short	2179
	.short	33030
	.short	33031
	.short	2243
	.short	33032
	.short	33033
	.short	33034
	.short	2307
	.short	33035
	.short	33036
	.short	2563
	.short	33037
	.short	33038
	.short	2627
	.short	33039
	.short	33040
	.short	2691
	.short	33041
	.short	33042
	.short	2755
	.short	33043
	.short	33044
	.short	2819
	.short	33045
	.short	33046
	.short	2050
	.short	33047
	.short	33048
	.short	33049
	.short	2114
	.short	33050
	.short	33051
	.short	2178
	.short	33052
	.short	33053
	.short	2242
	.short	33054
	.short	33055
	.short	2306
	.short	33056
	.short	33057
	.short	2562
	.short	33058
	.short	33059
	.short	2626
	.short	33060
	.short	33061
	.short	33062
	.short	2690
	.short	33063
	.short	33064
	.short	2754
	.short	33065
	.short	33066
	.short	2818
	.short	33067
	.short	33068
	.short	2049
	.short	33069
	.short	33070
	.short	2113
	.short	33071
	.short	33072
	.short	2177
	.short	33073
	.short	33074
	.short	2241
	.short	33075
	.short	33076
	.short	33077
	.short	2305
	.short	33078
	.short	33079
	.short	2561
	.short	33080
	.short	33081
	.short	2625
	.short	33082
	.short	33083
	.short	2689
	.short	33084
	.short	33085
	.short	2753
	.short	33086
	.short	33087
	.short	2817
	.short	33088
	.short	33089
	.short	33090
	.short	2048
	.short	33091
	.short	2112
	.short	33092
	.short	2176
	.short	33093
	.short	33094
	.short	2240
	.short	33095
	.short	2304
	.short	33096
	.short	33097
	.short	2560
	.short	33098
	.short	2624
	.short	33099
	.short	33100
	.short	2688
	.short	33101
	.short	2752
	.short	33102
	.short	2816
	.short	33103
	.short	33104
	.short	1039
	.short	33105
	.short	1103
	.short	33106
	.short	33107
	.short	1167
	.short	33108
	.short	1231
	.short	33109
	.short	33110
	.short	1295
	.short	33111
	.short	1551
	.short	33112
	.short	33113
	.short	1615
	.short	33114
	.short	1679
	.short	33115
	.short	1743
	.short	33116
	.short	33117
	.short	1807
	.short	33118
	.short	1038
	.short	33119
	.short	33120
	.short	1102
	.short	33121
	.short	1166
	.short	33122
	.short	33123
	.short	1230
	.short	33124
	.short	1294
	.short	33125
	.short	1550
	.short	33126
	.short	33127
	.short	1614
	.short	33128
	.short	1678
	.short	33129
	.short	33130
	.short	1742
	.short	33131
	.short	1806
	.short	33132
	.short	33133
	.short	1037
	.short	33134
	.short	1101
	.short	33135
	.short	1165
	.short	33136
	.short	33137
	.short	1229
	.short	33138
	.short	1293
	.short	33139
	.short	33140
	.short	1549
	.short	33141
	.short	1613
	.short	33142
	.short	33143
	.short	1677
	.short	33144
	.short	1741
	.short	33145
	.short	33146
	.short	1805
	.short	33147
	.short	1036
	.short	33148
	.short	1100
	.short	33149
	.short	33150
	.short	1164
	.short	33151
	.short	1228
	.short	33152
	.short	33153
	.short	1292
	.short	33154
	.short	1548
	.short	33155
	.short	33156
	.short	1612
	.short	33157
	.short	1676
	.short	33158
	.short	1740
	.short	33159
	.short	33160
	.short	1804
	.short	33161
	.short	1035
	.short	33162
	.short	33163
	.short	1099
	.short	33164
	.short	1163
	.short	33165
	.short	33166
	.short	1227
	.short	33167
	.short	1291
	.short	33168
	.short	33169
	.short	1547
	.short	33170
	.short	1611
	.short	33171
	.short	1675
	.short	33172
	.short	33173
	.short	1739
	.short	33174
	.short	1803
	.short	33175
	.short	33176
	.short	1034
	.short	33177
	.short	1098
	.short	33178
	.short	33179
	.short	1162
	.short	33180
	.short	1226
	.short	33181
	.short	1290
	.short	33182
	.short	33183
	.short	1546
	.short	33184
	.short	1610
	.short	33185
	.short	33186
	.short	1674
	.short	33187
	.short	1738
	.short	33188
	.short	33189
	.short	1802
	.short	33190
	.short	1033
	.short	33191
	.short	1097
	.short	33192
	.short	33193
	.short	1161
	.short	33194
	.short	1225
	.short	33195
	.short	33196
	.short	1289
	.short	33197
	.short	1545
	.short	33198
	.short	33199
	.short	1609
	.short	33200
	.short	1673
	.short	33201
	.short	33202
	.short	1737
	.short	33203
	.short	1801
	.short	33204
	.short	1032
	.short	33205
	.short	33206
	.short	1096
	.short	33207
	.short	1160
	.short	33208
	.short	33209
	.short	1224
	.short	33210
	.short	1288
	.short	33211
	.short	33212
	.short	1544
	.short	33213
	.short	1608
	.short	33214
	.short	1672
	.short	33215
	.short	33216
	.short	1736
	.short	33217
	.short	1800
	.short	33218
	.short	33219
	.short	1031
	.short	33220
	.short	1095
	.short	33221
	.short	33222
	.short	1159
	.short	33223
	.short	1223
	.short	33224
	.short	33225
	.short	1287
	.short	33226
	.short	1543
	.short	33227
	.short	1607
	.short	33228
	.short	33229
	.short	1671
	.short	33230
	.short	1735
	.short	33231
	.short	33232
	.short	1799
	.short	33233
	.short	1030
	.short	33234
	.short	33235
	.short	1094
	.short	33236
	.short	1158
	.short	33237
	.short	1222
	.short	33238
	.short	33239
	.short	1286
	.short	33240
	.short	1542
	.short	33241
	.short	33242
	.short	1606
	.short	33243
	.short	1670
	.short	33244
	.short	33245
	.short	1734
	.short	33246
	.short	1798
	.short	33247
	.short	1029
	.short	33248
	.short	33249
	.short	1093
	.short	33250
	.short	1157
	.short	33251
	.short	33252
	.short	1221
	.short	33253
	.short	1285
	.short	33254
	.short	33255
	.short	1541
	.short	33256
	.short	1605
	.short	33257
	.short	33258
	.short	1669
	.short	33259
	.short	1733
	.short	33260
	.short	1797
	.short	33261
	.short	33262
	.short	1028
	.short	33263
	.short	1092
	.short	33264
	.short	33265
	.short	1156
	.short	33266
	.short	1220
	.short	33267
	.short	33268
	.short	1284
	.short	33269
	.short	1540
	.short	33270
	.short	1604
	.short	33271
	.short	33272
	.short	1668
	.short	33273
	.short	1732
	.short	33274
	.short	33275
	.short	1796
	.short	33276
	.short	1027
	.short	33277
	.short	33278
	.short	1091
	.short	33279
	.short	1155
	.short	33280
	.short	33281
	.short	1219
	.short	33282
	.short	1283
	.short	33283
	.short	1539
	.short	33284
	.short	33285
	.short	1603
	.short	33286
	.short	1667
	.short	33287
	.short	33288
	.short	1731
	.short	33289
	.short	1795
	.short	33290
	.short	33291
	.short	1026
	.short	33292
	.short	1090
	.short	33293
	.short	1154
	.short	33294
	.short	33295
	.short	1218
	.short	33296
	.short	1282
	.short	33297
	.short	33298
	.short	1538
	.short	33299
	.short	1602
	.short	33300
	.short	33301
	.short	1666
	.short	33302
	.short	1730
	.short	33303
	.short	1794
	.short	33304
	.short	33305
	.short	1025
	.short	33306
	.short	1089
	.short	33307
	.short	33308
	.short	1153
	.short	33309
	.short	1217
	.short	33310
	.short	33311
	.short	1281
	.short	33312
	.short	1537
	.short	33313
	.short	33314
	.short	1601
	.short	33315
	.short	1665
	.short	33316
	.short	1729
	.short	33317
	.short	33318
	.short	1793
	.short	33319
	.short	1024
	.short	33320
	.short	33321
	.short	1088
	.short	33322
	.short	1152
	.short	33323
	.short	33324
	.short	1216
	.short	33325
	.short	1280
	.short	33326
	.short	1536
	.short	33327
	.short	33328
	.short	1600
	.short	33329
	.short	1664
	.short	33330
	.short	33331
	.short	1728
	.short	33332
	.short	1792
	.short	33333
	.short	33334
	.short	47
	.short	33335
	.short	111
	.short	33336
	.short	175
	.short	33337
	.short	33338
	.short	239
	.short	33339
	.short	303
	.short	33340
	.short	33341
	.short	367
	.short	33342
	.short	559
	.short	33343
	.short	33344
	.short	623
	.short	33345
	.short	687
	.short	33346
	.short	33347
	.short	751
	.short	33348
	.short	815
	.short	33349
	.short	879
	.short	33350
	.short	33351
	.short	46
	.short	33352
	.short	110
	.short	33353
	.short	33354
	.short	174
	.short	33355
	.short	238
	.short	33356
	.short	33357
	.short	302
	.short	33358
	.short	366
	.short	33359
	.short	558
	.short	33360
	.short	33361
	.short	622
	.short	33362
	.short	686
	.short	33363
	.short	33364
	.short	750
	.short	33365
	.short	814
	.short	33366
	.short	33367
	.short	878
	.short	33368
	.short	45
	.short	33369
	.short	33370
	.short	109
	.short	33371
	.short	173
	.short	33372
	.short	237
	.short	33373
	.short	33374
	.short	301
	.short	33375
	.short	365
	.short	33376
	.short	33377
	.short	557
	.short	33378
	.short	621
	.short	33379
	.short	33380
	.short	685
	.short	33381
	.short	749
	.short	33382
	.short	813
	.short	33383
	.short	33384
	.short	877
	.short	33385
	.short	44
	.short	33386
	.short	33387
	.short	108
	.short	33388
	.short	172
	.short	33389
	.short	33390
	.short	236
	.short	33391
	.short	300
	.short	33392
	.short	364
	.short	33393
	.short	33394
	.short	556
	.short	33395
	.short	620
	.short	33396
	.short	33397
	.short	684
	.short	33398
	.short	748
	.short	33399
	.short	33400
	.short	812
	.short	33401
	.short	876
	.short	33402
	.short	33403
	.short	43
	.short	33404
	.short	107
	.short	33405
	.short	171
	.short	33406
	.short	33407
	.short	235
	.short	33408
	.short	299
	.short	33409
	.short	33410
	.short	363
	.short	33411
	.short	555
	.short	33412
	.short	33413
	.short	619
	.short	33414
	.short	683
	.short	33415
	.short	747
	.short	33416
	.short	33417
	.short	811
	.short	33418
	.short	875
	.short	33419
	.short	33420
	.short	42
	.short	33421
	.short	106
	.short	33422
	.short	33423
	.short	170
	.short	33424
	.short	234
	.short	33425
	.short	33426
	.short	298
	.short	33427
	.short	362
	.short	33428
	.short	554
	.short	33429
	.short	33430
	.short	618
	.short	33431
	.short	682
	.short	33432
	.short	33433
	.short	746
	.short	33434
	.short	810
	.short	33435
	.short	33436
	.short	874
	.short	33437
	.short	41
	.short	33438
	.short	105
	.short	33439
	.short	33440
	.short	169
	.short	33441
	.short	233
	.short	33442
	.short	33443
	.short	297
	.short	33444
	.short	361
	.short	33445
	.short	33446
	.short	553
	.short	33447
	.short	617
	.short	33448
	.short	681
	.short	33449
	.short	33450
	.short	745
	.short	33451
	.short	809
	.short	33452
	.short	33453
	.short	873
	.short	33454
	.short	40
	.short	33455
	.short	33456
	.short	104
	.short	33457
	.short	168
	.short	33458
	.short	33459
	.short	232
	.short	33460
	.short	296
	.short	33461
	.short	360
	.short	33462
	.short	33463
	.short	552
	.short	33464
	.short	616
	.short	33465
	.short	33466
	.short	680
	.short	33467
	.short	744
	.short	33468
	.short	33469
	.short	808
	.short	33470
	.short	872
	.short	33471
	.short	39
	.short	33472
	.short	33473
	.short	103
	.short	33474
	.short	167
	.short	33475
	.short	33476
	.short	231
	.short	33477
	.short	295
	.short	33478
	.short	33479
	.short	359
	.short	33480
	.short	551
	.short	33481
	.short	33482
	.short	615
	.short	33483
	.short	679
	.short	33484
	.short	743
	.short	33485
	.short	33486
	.short	807
	.short	33487
	.short	871
	.short	33488
	.short	33489
	.short	38
	.short	33490
	.short	102
	.short	33491
	.short	33492
	.short	166
	.short	33493
	.short	230
	.short	33494
	.short	294
	.short	33495
	.short	33496
	.short	358
	.short	33497
	.short	550
	.short	33498
	.short	33499
	.short	614
	.short	33500
	.short	678
	.short	33501
	.short	33502
	.short	742
	.short	33503
	.short	806
	.short	33504
	.short	870
	.short	33505
	.short	33506
	.short	37
	.short	33507
	.short	101
	.short	33508
	.short	33509
	.short	165
	.short	33510
	.short	229
	.short	33511
	.short	33512
	.short	293
	.short	33513
	.short	357
	.short	33514
	.short	33515
	.short	549
	.short	33516
	.short	613
	.short	33517
	.short	677
	.short	33518
	.short	33519
	.short	741
	.short	33520
	.short	805
	.short	33521
	.short	33522
	.short	869
	.short	33523
	.short	36
	.short	33524
	.short	33525
	.short	100
	.short	33526
	.short	164
	.short	33527
	.short	228
	.short	33528
	.short	33529
	.short	292
	.short	33530
	.short	356
	.short	33531
	.short	33532
	.short	548
	.short	33533
	.short	612
	.short	33534
	.short	33535
	.short	676
	.short	33536
	.short	740
	.short	33537
	.short	33538
	.short	804
	.short	33539
	.short	868
	.short	33540
	.short	35
	.short	33541
	.short	33542
	.short	99
	.short	33543
	.short	163
	.short	33544
	.short	33545
	.short	227
	.short	33546
	.short	291
	.short	33547
	.short	33548
	.short	355
	.short	33549
	.short	547
	.short	33550
	.short	611
	.short	33551
	.short	33552
	.short	675
	.short	33553
	.short	739
	.short	33554
	.short	33555
	.short	803
	.short	33556
	.short	867
	.short	33557
	.short	33558
	.short	34
	.short	33559
	.short	98
	.short	33560
	.short	162
	.short	33561
	.short	33562
	.short	226
	.short	33563
	.short	290
	.short	33564
	.short	33565
	.short	354
	.short	33566
	.short	546
	.short	33567
	.short	33568
	.short	610
	.short	33569
	.short	674
	.short	33570
	.short	33571
	.short	738
	.short	33572
	.short	802
	.short	33573
	.short	866
	.short	33574
	.short	33575
	.short	33
	.short	33576
	.short	97
	.short	33577
	.short	33578
	.short	161
	.short	33579
	.short	225
	.short	33580
	.short	33581
	.short	289
	.short	33582
	.short	353
	.short	33583
	.short	545
	.short	33584
	.short	33585
	.short	609
	.short	33586
	.short	673
	.short	33587
	.short	33588
	.short	737
	.short	33589
	.short	801
	.short	33590
	.short	33591
	.short	865
	.short	33592
	.short	32
	.short	33593
	.short	96
	.short	33594
	.short	33595
	.short	160
	.short	33596
	.short	224
	.short	33597
	.short	33598
	.short	288
	.short	33599
	.short	352
	.short	33600
	.short	33601
	.short	544
	.short	33602
	.short	608
	.short	33603
	.short	33604
	.short	672
	.short	33605
	.short	736
	.short	33606
	.short	800
	.short	33607
	.short	33608
	.short	864
	.short	33609
	.short	31
	.short	33610
	.short	33611
	.short	95
	.short	33612
	.short	159
	.short	33613
	.short	33614
	.short	223
	.short	33615
	.short	287
	.short	33616
	.short	351
	.short	33617
	.short	33618
	.short	543
	.short	33619
	.short	607
	.short	33620
	.short	33621
	.short	671
	.short	33622
	.short	735
	.short	33623
	.short	33624
	.short	799
	.short	33625
	.short	863
	.short	33626
	.short	33627
	.short	30
	.short	33628
	.short	94
	.short	33629
	.short	158
	.short	33630
	.short	33631
	.short	222
	.short	33632
	.short	286
	.short	33633
	.short	33634
	.short	350
	.short	33635
	.short	542
	.short	33636
	.short	33637
	.short	606
	.short	33638
	.short	670
	.short	33639
	.short	734
	.short	33640
	.short	33641
	.short	798
	.short	33642
	.short	862
	.short	33643
	.short	33644
	.short	29
	.short	33645
	.short	93
	.short	33646
	.short	33647
	.short	157
	.short	33648
	.short	221
	.short	33649
	.short	285
	.short	33650
	.short	33651
	.short	349
	.short	33652
	.short	541
	.short	33653
	.short	33654
	.short	605
	.short	33655
	.short	669
	.short	33656
	.short	33657
	.short	733
	.short	33658
	.short	797
	.short	33659
	.short	33660
	.short	861
	.short	33661
	.short	28
	.short	33662
	.short	92
	.short	33663
	.short	33664
	.short	156
	.short	33665
	.short	220
	.short	33666
	.short	33667
	.short	284
	.short	33668
	.short	348
	.short	33669
	.short	33670
	.short	540
	.short	33671
	.short	604
	.short	33672
	.short	668
	.short	33673
	.short	33674
	.short	732
	.short	33675
	.short	796
	.short	33676
	.short	33677
	.short	860
	.short	33678
	.short	27
	.short	33679
	.short	33680
	.short	91
	.short	33681
	.short	155
	.short	33682
	.short	33683
	.short	219
	.short	33684
	.short	283
	.short	33685
	.short	347
	.short	33686
	.short	33687
	.short	539
	.short	33688
	.short	603
	.short	33689
	.short	33690
	.short	667
	.short	33691
	.short	731
	.short	33692
	.short	33693
	.short	795
	.short	33694
	.short	859
	.short	33695
	.short	26
	.short	33696
	.short	33697
	.short	90
	.short	33698
	.short	154
	.short	33699
	.short	33700
	.short	218
	.short	33701
	.short	282
	.short	33702
	.short	33703
	.short	346
	.short	33704
	.short	538
	.short	33705
	.short	602
	.short	33706
	.short	33707
	.short	666
	.short	33708
	.short	730
	.short	33709
	.short	33710
	.short	794
	.short	33711
	.short	858
	.short	33712
	.short	33713
	.short	25
	.short	33714
	.short	89
	.short	33715
	.short	33716
	.short	153
	.short	33717
	.short	217
	.short	33718
	.short	281
	.short	33719
	.short	33720
	.short	345
	.short	33721
	.short	537
	.short	33722
	.short	33723
	.short	601
	.short	33724
	.short	665
	.short	33725
	.short	33726
	.short	729
	.short	33727
	.short	793
	.short	33728
	.short	857
	.short	33729
	.short	33730
	.short	24
	.short	33731
	.short	88
	.short	33732
	.short	33733
	.short	152
	.short	33734
	.short	216
	.short	33735
	.short	33736
	.short	280
	.short	33737
	.short	344
	.short	33738
	.short	33739
	.short	536
	.short	33740
	.short	600
	.short	33741
	.short	664
	.short	33742
	.short	33743
	.short	728
	.short	33744
	.short	792
	.short	33745
	.short	33746
	.short	856
	.short	33747
	.short	23
	.short	33748
	.short	33749
	.short	87
	.short	33750
	.short	151
	.short	33751
	.short	215
	.short	33752
	.short	33753
	.short	279
	.short	33754
	.short	343
	.short	33755
	.short	33756
	.short	535
	.short	33757
	.short	599
	.short	33758
	.short	33759
	.short	663
	.short	33760
	.short	727
	.short	33761
	.short	791
	.short	33762
	.short	33763
	.short	855
	.short	33764
	.short	22
	.short	33765
	.short	33766
	.short	86
	.short	33767
	.short	150
	.short	33768
	.short	33769
	.short	214
	.short	33770
	.short	278
	.short	33771
	.short	33772
	.short	342
	.short	33773
	.short	534
	.short	33774
	.short	598
	.short	33775
	.short	33776
	.short	662
	.short	33777
	.short	726
	.short	33778
	.short	33779
	.short	790
	.short	33780
	.short	854
	.short	33781
	.short	33782
	.short	21
	.short	33783
	.short	85
	.short	33784
	.short	149
	.short	33785
	.short	33786
	.short	213
	.short	33787
	.short	277
	.short	33788
	.short	33789
	.short	341
	.short	33790
	.short	533
	.short	33791
	.short	33792
	.short	597
	.short	33793
	.short	661
	.short	33794
	.short	33795
	.short	725
	.short	33796
	.short	789
	.short	33797
	.short	853
	.short	33798
	.short	33799
	.short	20
	.short	33800
	.short	84
	.short	33801
	.short	33802
	.short	148
	.short	33803
	.short	212
	.short	33804
	.short	33805
	.short	276
	.short	33806
	.short	340
	.short	33807
	.short	532
	.short	33808
	.short	33809
	.short	596
	.short	33810
	.short	660
	.short	33811
	.short	33812
	.short	724
	.short	33813
	.short	788
	.short	33814
	.short	33815
	.short	852
	.short	33816
	.short	19
	.short	33817
	.short	83
	.short	33818
	.short	33819
	.short	147
	.short	33820
	.short	211
	.short	33821
	.short	33822
	.short	275
	.short	33823
	.short	339
	.short	33824
	.short	33825
	.short	531
	.short	33826
	.short	595
	.short	33827
	.short	33828
	.short	659
	.short	33829
	.short	723
	.short	33830
	.short	787
	.short	33831
	.short	33832
	.short	851
	.short	33833
	.short	18
	.short	33834
	.short	33835
	.short	82
	.short	33836
	.short	146
	.short	33837
	.short	33838
	.short	210
	.short	33839
	.short	274
	.short	33840
	.short	338
	.short	33841
	.short	33842
	.short	530
	.short	33843
	.short	594
	.short	33844
	.short	33845
	.short	658
	.short	33846
	.short	722
	.short	33847
	.short	33848
	.short	786
	.short	33849
	.short	850
	.short	33850
	.short	17
	.short	33851
	.short	33852
	.short	81
	.short	33853
	.short	145
	.short	33854
	.short	33855
	.short	209
	.short	33856
	.short	273
	.short	33857
	.short	33858
	.short	337
	.short	33859
	.short	529
	.short	33860
	.short	33861
	.short	593
	.short	33862
	.short	657
	.short	33863
	.short	721
	.short	33864
	.short	33865
	.short	785
	.short	33866
	.short	849
	.short	33867
	.short	33868
	.short	16
	.short	33869
	.short	80
	.short	33870
	.short	33871
	.short	144
	.short	33872
	.short	208
	.short	33873
	.short	272
	.short	33874
	.short	33875
	.short	336
	.short	33876
	.short	528
	.short	33877
	.short	33878
	.short	592
	.short	33879
	.short	656
	.short	33880
	.short	33881
	.short	720
	.short	33882
	.short	784
	.short	33883
	.short	33884
	.short	848
	.short	33885
	.short	15
	.short	33886
	.short	79
	.short	33887
	.short	33888
	.short	143
	.short	33889
	.short	207
	.short	33890
	.short	33891
	.short	271
	.short	33892
	.short	335
	.short	33893
	.short	33894
	.short	527
	.short	33895
	.short	591
	.short	33896
	.short	655
	.short	33897
	.short	33898
	.short	719
	.short	33899
	.short	783
	.short	33900
	.short	33901
	.short	847
	.short	33902
	.short	14
	.short	33903
	.short	33904
	.short	78
	.short	33905
	.short	142
	.short	33906
	.short	206
	.short	33907
	.short	33908
	.short	270
	.short	33909
	.short	334
	.short	33910
	.short	33911
	.short	526
	.short	33912
	.short	590
	.short	33913
	.short	33914
	.short	654
	.short	33915
	.short	718
	.short	33916
	.short	33917
	.short	782
	.short	33918
	.short	846
	.short	33919
	.short	13
	.short	33920
	.short	33921
	.short	77
	.short	33922
	.short	141
	.short	33923
	.short	33924
	.short	205
	.short	33925
	.short	269
	.short	33926
	.short	33927
	.short	333
	.short	33928
	.short	525
	.short	33929
	.short	589
	.short	33930
	.short	33931
	.short	653
	.short	33932
	.short	717
	.short	33933
	.short	33934
	.short	781
	.short	33935
	.short	845
	.short	33936
	.short	33937
	.short	12
	.short	33938
	.short	76
	.short	33939
	.short	33940
	.short	140
	.short	33941
	.short	204
	.short	33942
	.short	268
	.short	33943
	.short	33944
	.short	332
	.short	33945
	.short	524
	.short	33946
	.short	33947
	.short	588
	.short	33948
	.short	652
	.short	33949
	.short	33950
	.short	716
	.short	33951
	.short	780
	.short	33952
	.short	844
	.short	33953
	.short	33954
	.short	11
	.short	33955
	.short	75
	.short	33956
	.short	33957
	.short	139
	.short	33958
	.short	203
	.short	33959
	.short	33960
	.short	267
	.short	33961
	.short	331
	.short	33962
	.short	523
	.short	33963
	.short	33964
	.short	587
	.short	33965
	.short	651
	.short	33966
	.short	33967
	.short	715
	.short	33968
	.short	779
	.short	33969
	.short	33970
	.short	843
	.short	33971
	.short	10
	.short	33972
	.short	33973
	.short	74
	.short	33974
	.short	138
	.short	33975
	.short	202
	.short	33976
	.short	33977
	.short	266
	.short	33978
	.short	330
	.short	33979
	.short	33980
	.short	522
	.short	33981
	.short	586
	.short	33982
	.short	33983
	.short	650
	.short	33984
	.short	714
	.short	33985
	.short	778
	.short	33986
	.short	33987
	.short	842
	.short	33988
	.short	9
	.short	33989
	.short	33990
	.short	73
	.short	33991
	.short	137
	.short	33992
	.short	33993
	.short	201
	.short	33994
	.short	265
	.short	33995
	.short	33996
	.short	329
	.short	33997
	.short	521
	.short	33998
	.short	585
	.short	33999
	.short	34000
	.short	649
	.short	34001
	.short	713
	.short	34002
	.short	34003
	.short	777
	.short	34004
	.short	841
	.short	34005
	.short	34006
	.short	8
	.short	34007
	.short	72
	.short	34008
	.short	136
	.short	34009
	.short	34010
	.short	200
	.short	34011
	.short	264
	.short	34012
	.short	34013
	.short	328
	.short	34014
	.short	520
	.short	34015
	.short	34016
	.short	584
	.short	34017
	.short	648
	.short	34018
	.short	712
	.short	34019
	.short	34020
	.short	776
	.short	34021
	.short	840
	.short	34022
	.short	34023
	.short	7
	.short	34024
	.short	71
	.short	34025
	.short	34026
	.short	135
	.short	34027
	.short	199
	.short	34028
	.short	34029
	.short	263
	.short	34030
	.short	327
	.short	34031
	.short	519
	.short	34032
	.short	34033
	.short	583
	.short	34034
	.short	647
	.short	34035
	.short	34036
	.short	711
	.short	34037
	.short	775
	.short	34038
	.short	34039
	.short	839
	.short	34040
	.short	6
	.short	34041
	.short	70
	.short	34042
	.short	34043
	.short	134
	.short	34044
	.short	198
	.short	34045
	.short	34046
	.short	262
	.short	34047
	.short	326
	.short	34048
	.short	34049
	.short	518
	.short	34050
	.short	582
	.short	34051
	.short	34052
	.short	646
	.short	34053
	.short	710
	.short	34054
	.short	774
	.short	34055
	.short	34056
	.short	838
	.short	34057
	.short	5
	.short	34058
	.short	34059
	.short	69
	.short	34060
	.short	133
	.short	34061
	.short	34062
	.short	197
	.short	34063
	.short	261
	.short	34064
	.short	325
	.short	34065
	.short	34066
	.short	517
	.short	34067
	.short	581
	.short	34068
	.short	34069
	.short	645
	.short	34070
	.short	709
	.short	34071
	.short	34072
	.short	773
	.short	34073
	.short	837
	.short	34074
	.short	4
	.short	34075
	.short	34076
	.short	68
	.short	34077
	.short	132
	.short	34078
	.short	34079
	.short	196
	.short	34080
	.short	260
	.short	34081
	.short	34082
	.short	324
	.short	34083
	.short	516
	.short	34084
	.short	34085
	.short	580
	.short	34086
	.short	644
	.short	34087
	.short	708
	.short	34088
	.short	34089
	.short	772
	.short	34090
	.short	836
	.short	34091
	.short	34092
	.short	3
	.short	34093
	.short	67
	.short	34094
	.short	34095
	.short	131
	.short	34096
	.short	195
	.short	34097
	.short	259
	.short	34098
	.short	34099
	.short	323
	.short	34100
	.short	515
	.short	34101
	.short	34102
	.short	579
	.short	34103
	.short	643
	.short	34104
	.short	34105
	.short	707
	.short	34106
	.short	771
	.short	34107
	.short	835
	.short	34108
	.short	34109
	.short	2
	.short	34110
	.short	66
	.short	34111
	.short	34112
	.short	130
	.short	34113
	.short	194
	.short	34114
	.short	34115
	.short	258
	.short	34116
	.short	322
	.short	34117
	.short	34118
	.short	514
	.short	34119
	.short	578
	.short	34120
	.short	642
	.short	34121
	.short	34122
	.short	706
	.short	34123
	.short	770
	.short	34124
	.short	34125
	.short	834
	.short	34126
	.short	1
	.short	34127
	.short	34128
	.short	65
	.short	34129
	.short	129
	.short	34130
	.short	193
	.short	34131
	.short	34132
	.short	257
	.short	34133
	.short	321
	.short	34134
	.short	34135
	.short	513
	.short	34136
	.short	577
	.short	34137
	.short	34138
	.short	641
	.short	34139
	.short	705
	.short	34140
	.short	34141
	.short	769
	.short	34142
	.short	833
	.short	34143
	.short	0
	.short	34144
	.short	34145
	.short	64
	.short	34146
	.short	128
	.short	34147
	.short	34148
	.short	192
	.short	34149
	.short	256
	.short	34150
	.short	34151
	.short	320
	.short	34152
	.short	512
	.short	34153
	.short	576
	.short	34154
	.short	34155
	.short	640
	.short	34156
	.short	704
	.short	34157
	.short	34158
	.short	768
	.short	34159
	.short	832
	.short	34160
	.short	34161
	.short	16384
	.short	34162
	.short	16640
	.short	34163
	.short	16896
	.short	34164
	.short	34165
	.short	17152
	.short	34166
	.short	17408
	.short	34167
	.short	34168
	.short	18432
	.short	34169
	.short	18688
	.short	34170
	.short	34171
	.short	18944
	.short	34172
	.short	19200
	.short	34173
	.short	34174
	.short	19456
	.short	34175
	.short	16400
	.short	34176
	.short	16656
	.short	34177
	.short	34178
	.short	16912
	.short	34179
	.short	17168
	.short	34180
	.short	34181
	.short	17424
	.short	34182
	.short	18448
	.short	34183
	.short	34184
	.short	18704
	.short	34185
	.short	18960
	.short	34186
	.short	19216
	.short	34187
	.short	34188
	.short	19472
	.short	34189
	.short	16416
	.short	34190
	.short	34191
	.short	16672
	.short	34192
	.short	16928
	.short	34193
	.short	34194
	.short	17184
	.short	34195
	.short	17440
	.short	34196
	.short	34197
	.short	18464
	.short	34198
	.short	18720
	.short	34199
	.short	18976
	.short	34200
	.short	34201
	.short	19232
	.short	34202
	.short	19488
	.short	34203
	.short	34204
	.short	16432
	.short	34205
	.short	16688
	.short	34206
	.short	34207
	.short	16944
	.short	34208
	.short	17200
	.short	34209
	.short	17456
	.short	34210
	.short	34211
	.short	18480
	.short	34212
	.short	18736
	.short	34213
	.short	34214
	.short	18992
	.short	34215
	.short	19248
	.short	34216
	.short	34217
	.short	19504
	.short	34218
	.short	16448
	.short	34219
	.short	16704
	.short	34220
	.short	34221
	.short	16960
	.short	34222
	.short	17216
	.short	34223
	.short	34224
	.short	17472
	.short	34225
	.short	18496
	.short	34226
	.short	34227
	.short	18752
	.short	34228
	.short	19008
	.short	34229
	.short	34230
	.short	19264
	.short	34231
	.short	19520
	.short	34232
	.short	16464
	.short	34233
	.short	34234
	.short	16720
	.short	34235
	.short	16976
	.short	34236
	.short	34237
	.short	17232
	.short	34238
	.short	17488
	.short	34239
	.short	34240
	.short	18512
	.short	34241
	.short	18768
	.short	34242
	.short	19024
	.short	34243
	.short	34244
	.short	19280
	.short	34245
	.short	19536
	.short	34246
	.short	34247
	.short	16480
	.short	34248
	.short	16736
	.short	34249
	.short	34250
	.short	16992
	.short	34251
	.short	17248
	.short	34252
	.short	34253
	.short	17504
	.short	34254
	.short	18528
	.short	34255
	.short	18784
	.short	34256
	.short	34257
	.short	19040
	.short	34258
	.short	19296
	.short	34259
	.short	34260
	.short	19552
	.short	34261
	.short	16496
	.short	34262
	.short	34263
	.short	16752
	.short	34264
	.short	17008
	.short	34265
	.short	17264
	.short	34266
	.short	34267
	.short	17520
	.short	34268
	.short	18544
	.short	34269
	.short	34270
	.short	18800
	.short	34271
	.short	19056
	.short	34272
	.short	34273
	.short	19312
	.short	34274
	.short	19568
	.short	34275
	.short	16512
	.short	34276
	.short	34277
	.short	16768
	.short	34278
	.short	17024
	.short	34279
	.short	34280
	.short	17280
	.short	34281
	.short	17536
	.short	34282
	.short	34283
	.short	18560
	.short	34284
	.short	18816
	.short	34285
	.short	34286
	.short	19072
	.short	34287
	.short	19328
	.short	34288
	.short	19584
	.short	34289
	.short	34290
	.short	16528
	.short	34291
	.short	16784
	.short	34292
	.short	34293
	.short	17040
	.short	34294
	.short	17296
	.short	34295
	.short	34296
	.short	17552
	.short	34297
	.short	18576
	.short	34298
	.short	18832
	.short	34299
	.short	34300
	.short	19088
	.short	34301
	.short	19344
	.short	34302
	.short	34303
	.short	19600
	.short	34304
	.short	16544
	.short	34305
	.short	34306
	.short	16800
	.short	34307
	.short	17056
	.short	34308
	.short	34309
	.short	17312
	.short	34310
	.short	17568
	.short	34311
	.short	18592
	.short	34312
	.short	34313
	.short	18848
	.short	34314
	.short	19104
	.short	34315
	.short	34316
	.short	19360
	.short	34317
	.short	19616
	.short	34318
	.short	34319
	.short	16560
	.short	34320
	.short	16816
	.short	34321
	.short	17072
	.short	34322
	.short	34323
	.short	17328
	.short	34324
	.short	17584
	.short	34325
	.short	34326
	.short	18608
	.short	34327
	.short	18864
	.short	34328
	.short	34329
	.short	19120
	.short	34330
	.short	19376
	.short	34331
	.short	19632
	.short	34332
	.short	34333
	.short	16576
	.short	34334
	.short	16832
	.short	34335
	.short	34336
	.short	17088
	.short	34337
	.short	17344
	.short	34338
	.short	34339
	.short	17600
	.short	34340
	.short	18624
	.short	34341
	.short	34342
	.short	18880
	.short	34343
	.short	19136
	.short	34344
	.short	19392
	.short	34345
	.short	34346
	.short	19648
	.short	34347
	.short	16592
	.short	34348
	.short	34349
	.short	16848
	.short	34350
	.short	17104
	.short	34351
	.short	34352
	.short	17360
	.short	34353
	.short	17616
	.short	34354
	.short	18640
	.short	34355
	.short	34356
	.short	18896
	.short	34357
	.short	19152
	.short	34358
	.short	34359
	.short	19408
	.short	34360
	.short	19664
	.short	34361
	.short	34362
	.short	16608
	.short	34363
	.short	16864
	.short	34364
	.short	17120
	.short	34365
	.short	34366
	.short	17376
	.short	34367
	.short	17632
	.short	34368
	.short	34369
	.short	18656
	.short	34370
	.short	18912
	.short	34371
	.short	34372
	.short	19168
	.short	34373
	.short	19424
	.short	34374
	.short	34375
	.short	19680
	.short	34376
	.short	16385
	.short	34377
	.short	16641
	.short	34378
	.short	34379
	.short	16897
	.short	34380
	.short	17153
	.short	34381
	.short	34382
	.short	17409
	.short	34383
	.short	18433
	.short	34384
	.short	34385
	.short	18689
	.short	34386
	.short	18945
	.short	34387
	.short	19201
	.short	34388
	.short	34389
	.short	19457
	.short	34390
	.short	16401
	.short	34391
	.short	34392
	.short	16657
	.short	34393
	.short	16913
	.short	34394
	.short	34395
	.short	17169
	.short	34396
	.short	17425
	.short	34397
	.short	34398
	.short	18449
	.short	34399
	.short	18705
	.short	34400
	.short	18961
	.short	34401
	.short	34402
	.short	19217
	.short	34403
	.short	19473
	.short	34404
	.short	34405
	.short	16417
	.short	34406
	.short	16673
	.short	34407
	.short	34408
	.short	16929
	.short	34409
	.short	17185
	.short	34410
	.short	17441
	.short	34411
	.short	34412
	.short	18465
	.short	34413
	.short	18721
	.short	34414
	.short	34415
	.short	18977
	.short	34416
	.short	19233
	.short	34417
	.short	34418
	.short	19489
	.short	34419
	.short	16433
	.short	34420
	.short	16689
	.short	34421
	.short	34422
	.short	16945
	.short	34423
	.short	17201
	.short	34424
	.short	34425
	.short	17457
	.short	34426
	.short	18481
	.short	34427
	.short	34428
	.short	18737
	.short	34429
	.short	18993
	.short	34430
	.short	34431
	.short	19249
	.short	34432
	.short	19505
	.short	34433
	.short	16449
	.short	34434
	.short	34435
	.short	16705
	.short	34436
	.short	16961
	.short	34437
	.short	34438
	.short	17217
	.short	34439
	.short	17473
	.short	34440
	.short	34441
	.short	18497
	.short	34442
	.short	18753
	.short	34443
	.short	19009
	.short	34444
	.short	34445
	.short	19265
	.short	34446
	.short	19521
	.short	34447
	.short	34448
	.short	16465
	.short	34449
	.short	16721
	.short	34450
	.short	34451
	.short	16977
	.short	34452
	.short	17233
	.short	34453
	.short	34454
	.short	17489
	.short	34455
	.short	18513
	.short	34456
	.short	18769
	.short	34457
	.short	34458
	.short	19025
	.short	34459
	.short	19281
	.short	34460
	.short	34461
	.short	19537
	.short	34462
	.short	16481
	.short	34463
	.short	34464
	.short	16737
	.short	34465
	.short	16993
	.short	34466
	.short	17249
	.short	34467
	.short	34468
	.short	17505
	.short	34469
	.short	18529
	.short	34470
	.short	34471
	.short	18785
	.short	34472
	.short	19041
	.short	34473
	.short	34474
	.short	19297
	.short	34475
	.short	19553
	.short	34476
	.short	16497
	.short	34477
	.short	34478
	.short	16753
	.short	34479
	.short	17009
	.short	34480
	.short	34481
	.short	17265
	.short	34482
	.short	17521
	.short	34483
	.short	34484
	.short	18545
	.short	34485
	.short	18801
	.short	34486
	.short	34487
	.short	19057
	.short	34488
	.short	19313
	.short	34489
	.short	19569
	.short	34490
	.short	34491
	.short	16513
	.short	34492
	.short	16769
	.short	34493
	.short	34494
	.short	17025
	.short	34495
	.short	17281
	.short	34496
	.short	34497
	.short	17537
	.short	34498
	.short	18561
	.short	34499
	.short	18817
	.short	34500
	.short	34501
	.short	19073
	.short	34502
	.short	19329
	.short	34503
	.short	34504
	.short	19585
	.short	34505
	.short	16529
	.short	34506
	.short	34507
	.short	16785
	.short	34508
	.short	17041
	.short	34509
	.short	34510
	.short	17297
	.short	34511
	.short	17553
	.short	34512
	.short	18577
	.short	34513
	.short	34514
	.short	18833
	.short	34515
	.short	19089
	.short	34516
	.short	34517
	.short	19345
	.short	34518
	.short	19601
	.short	34519
	.short	34520
	.short	16545
	.short	34521
	.short	16801
	.short	34522
	.short	17057
	.short	34523
	.short	34524
	.short	17313
	.short	34525
	.short	17569
	.short	34526
	.short	34527
	.short	18593
	.short	34528
	.short	18849
	.short	34529
	.short	34530
	.short	19105
	.short	34531
	.short	19361
	.short	34532
	.short	19617
	.short	34533
	.short	34534
	.short	16386
	.short	34535
	.short	16642
	.short	34536
	.short	34537
	.short	16898
	.short	34538
	.short	17154
	.short	34539
	.short	34540
	.short	17410
	.short	34541
	.short	18434
	.short	34542
	.short	34543
	.short	18690
	.short	34544
	.short	18946
	.short	34545
	.short	19202
	.short	34546
	.short	34547
	.short	19458
	.short	34548
	.short	16402
	.short	34549
	.short	34550
	.short	16658
	.short	34551
	.short	16914
	.short	34552
	.short	34553
	.short	17170
	.short	34554
	.short	17426
	.short	34555
	.short	18450
	.short	34556
	.short	34557
	.short	18706
	.short	34558
	.short	18962
	.short	34559
	.short	34560
	.short	19218
	.short	34561
	.short	19474
	.short	34562
	.short	34563
	.short	16418
	.short	34564
	.short	16674
	.short	34565
	.short	34566
	.short	16930
	.short	34567
	.short	17186
	.short	34568
	.short	17442
	.short	34569
	.short	34570
	.short	18466
	.short	34571
	.short	18722
	.short	34572
	.short	34573
	.short	18978
	.short	34574
	.short	19234
	.short	34575
	.short	34576
	.short	19490
	.short	34577
	.short	16434
	.short	34578
	.short	16690
	.short	34579
	.short	34580
	.short	16946
	.short	34581
	.short	17202
	.short	34582
	.short	34583
	.short	17458
	.short	34584
	.short	18482
	.short	34585
	.short	34586
	.short	18738
	.short	34587
	.short	18994
	.short	34588
	.short	19250
	.short	34589
	.short	34590
	.short	19506
	.short	34591
	.short	16450
	.short	34592
	.short	34593
	.short	16706
	.short	34594
	.short	16962
	.short	34595
	.short	34596
	.short	17218
	.short	34597
	.short	17474
	.short	34598
	.short	34599
	.short	18498
	.short	34600
	.short	18754
	.short	34601
	.short	19010
	.short	34602
	.short	34603
	.short	19266
	.short	34604
	.short	19522
	.short	34605
	.short	34606
	.short	16466
	.short	34607
	.short	16722
	.short	34608
	.short	34609
	.short	16978
	.short	34610
	.short	17234
	.short	34611
	.short	17490
	.short	34612
	.short	34613
	.short	18514
	.short	34614
	.short	18770
	.short	34615
	.short	34616
	.short	19026
	.short	34617
	.short	19282
	.short	34618
	.short	34619
	.short	19538
	.short	34620
	.short	16482
	.short	34621
	.short	16738
	.short	34622
	.short	34623
	.short	16994
	.short	34624
	.short	17250
	.short	34625
	.short	34626
	.short	17506
	.short	34627
	.short	18530
	.short	34628
	.short	34629
	.short	18786
	.short	34630
	.short	19042
	.short	34631
	.short	34632
	.short	19298
	.short	34633
	.short	19554
	.short	34634
	.short	16498
	.short	34635
	.short	34636
	.short	16754
	.short	34637
	.short	17010
	.short	34638
	.short	34639
	.short	17266
	.short	34640
	.short	17522
	.short	34641
	.short	34642
	.short	18546
	.short	34643
	.short	18802
	.short	34644
	.short	19058
	.short	34645
	.short	34646
	.short	19314
	.short	34647
	.short	19570
	.short	34648
	.short	34649
	.short	16387
	.short	34650
	.short	16643
	.short	34651
	.short	34652
	.short	16899
	.short	34653
	.short	17155
	.short	34654
	.short	34655
	.short	17411
	.short	34656
	.short	18435
	.short	34657
	.short	18691
	.short	34658
	.short	34659
	.short	18947
	.short	34660
	.short	19203
	.short	34661
	.short	34662
	.short	19459
	.short	34663
	.short	16403
	.short	34664
	.short	34665
	.short	16659
	.short	34666
	.short	16915
	.short	34667
	.short	17171
	.short	34668
	.short	34669
	.short	17427
	.short	34670
	.short	18451
	.short	34671
	.short	34672
	.short	18707
	.short	34673
	.short	18963
	.short	34674
	.short	34675
	.short	19219
	.short	34676
	.short	19475
	.short	34677
	.short	16419
	.short	34678
	.short	34679
	.short	16675
	.short	34680
	.short	16931
	.short	34681
	.short	34682
	.short	17187
	.short	34683
	.short	17443
	.short	34684
	.short	34685
	.short	18467
	.short	34686
	.short	18723
	.short	34687
	.short	34688
	.short	18979
	.short	34689
	.short	19235
	.short	34690
	.short	19491
	.short	34691
	.short	34692
	.short	16435
	.short	34693
	.short	16691
	.short	34694
	.short	34695
	.short	16947
	.short	34696
	.short	17203
	.short	34697
	.short	34698
	.short	17459
	.short	34699
	.short	18483
	.short	34700
	.short	18739
	.short	34701
	.short	34702
	.short	18995
	.short	34703
	.short	19251
	.short	34704
	.short	34705
	.short	19507
	.short	34706
	.short	16451
	.short	34707
	.short	34708
	.short	16707
	.short	34709
	.short	16963
	.short	34710
	.short	34711
	.short	17219
	.short	34712
	.short	17475
	.short	34713
	.short	18499
	.short	34714
	.short	34715
	.short	18755
	.short	34716
	.short	19011
	.short	34717
	.short	34718
	.short	19267
	.short	34719
	.short	19523
	.short	34720
	.short	34721
	.short	16467
	.short	34722
	.short	16723
	.short	34723
	.short	16979
	.short	34724
	.short	34725
	.short	17235
	.short	34726
	.short	17491
	.short	34727
	.short	34728
	.short	18515
	.short	34729
	.short	18771
	.short	34730
	.short	34731
	.short	19027
	.short	34732
	.short	19283
	.short	34733
	.short	19539
	.short	34734
	.short	34735
	.short	16388
	.short	34736
	.short	16644
	.short	34737
	.short	34738
	.short	16900
	.short	34739
	.short	17156
	.short	34740
	.short	34741
	.short	17412
	.short	34742
	.short	18436
	.short	34743
	.short	34744
	.short	18692
	.short	34745
	.short	18948
	.short	34746
	.short	19204
	.short	34747
	.short	34748
	.short	19460
	.short	34749
	.short	16404
	.short	34750
	.short	34751
	.short	16660
	.short	34752
	.short	16916
	.short	34753
	.short	34754
	.short	17172
	.short	34755
	.short	17428
	.short	34756
	.short	18452
	.short	34757
	.short	34758
	.short	18708
	.short	34759
	.short	18964
	.short	34760
	.short	34761
	.short	19220
	.short	34762
	.short	19476
	.short	34763
	.short	34764
	.short	16420
	.short	34765
	.short	16676
	.short	34766
	.short	34767
	.short	16932
	.short	34768
	.short	17188
	.short	34769
	.short	17444
	.short	34770
	.short	34771
	.short	18468
	.short	34772
	.short	18724
	.short	34773
	.short	34774
	.short	18980
	.short	34775
	.short	19236
	.short	34776
	.short	34777
	.short	19492
	.short	34778
	.short	16436
	.short	34779
	.short	16692
	.short	34780
	.short	34781
	.short	16948
	.short	34782
	.short	17204
	.short	34783
	.short	34784
	.short	17460
	.short	34785
	.short	18484
	.short	34786
	.short	34787
	.short	18740
	.short	34788
	.short	18996
	.short	34789
	.short	19252
	.short	34790
	.short	34791
	.short	19508
	.short	34792
	.short	16389
	.short	34793
	.short	34794
	.short	16645
	.short	34795
	.short	16901
	.short	34796
	.short	34797
	.short	17157
	.short	34798
	.short	17413
	.short	34799
	.short	34800
	.short	18437
	.short	34801
	.short	18693
	.short	34802
	.short	18949
	.short	34803
	.short	34804
	.short	19205
	.short	34805
	.short	19461
	.short	34806
	.short	34807
	.short	16405
	.short	34808
	.short	16661
	.short	34809
	.short	34810
	.short	16917
	.short	34811
	.short	17173
	.short	34812
	.short	17429
	.short	34813
	.short	34814
	.short	18453
	.short	34815
	.short	18709
	.short	34816
	.short	34817
	.short	18965
	.short	34818
	.short	19221
	.short	34819
	.short	34820
	.short	19477
	.short	34821
	.short	16421
	.short	34822
	.short	34823
	.short	16677
	.short	34824
	.short	16933
	.short	34825
	.short	17189
	.short	34826
	.short	34827
	.short	17445
	.short	34828
	.short	18469
	.short	34829
	.short	34830
	.short	18725
	.short	34831
	.short	18981
	.short	34832
	.short	34833
	.short	19237
	.short	34834
	.short	19493
	.short	34835
	.short	16390
	.short	34836
	.short	34837
	.short	16646
	.short	34838
	.short	16902
	.short	34839
	.short	34840
	.short	17158
	.short	34841
	.short	17414
	.short	34842
	.short	34843
	.short	18438
	.short	34844
	.short	18694
	.short	34845
	.short	18950
	.short	34846
	.short	34847
	.short	19206
	.short	34848
	.short	19462
	.short	34849
	.short	34850
	.short	16406
	.short	34851
	.short	16662
	.short	34852
	.short	34853
	.short	16918
	.short	34854
	.short	17174
	.short	34855
	.short	34856
	.short	17430
	.short	34857
	.short	18454
	.short	34858
	.short	18710
	.short	34859
	.short	34860
	.short	18966
	.short	34861
	.short	19222
	.short	34862
	.short	34863
	.short	19478
	.short	34864
	.short	16391
	.short	34865
	.short	34866
	.short	16647
	.short	34867
	.short	16903
	.short	34868
	.short	17159
	.short	34869
	.short	34870
	.short	17415
	.short	34871
	.short	18439
	.short	34872
	.short	34873
	.short	18695
	.short	34874
	.short	18951
	.short	34875
	.short	34876
	.short	19207
	.short	34877
	.short	19463
	.short	34878
	.short	34879
	.short	20657
	.short	20913
	.short	21169
	.short	21425
	.short	21681
	.short	22705
	.short	22961
	.short	23217
	.short	23473
	.short	23729
	.short	20673
	.short	20929
	.short	21185
	.short	21441
	.short	21697
	.short	22721
	.short	22977
	.short	23233
	.short	23489
	.short	23745
	.short	20689
	.short	20945
	.short	21201
	.short	21457
	.short	21713
	.short	22737
	.short	22993
	.short	23249
	.short	23505
	.short	23761
	.short	20610
	.short	20866
	.short	21122
	.short	21378
	.short	21634
	.short	22658
	.short	22914
	.short	23170
	.short	23426
	.short	23682
	.short	20626
	.short	20882
	.short	21138
	.short	21394
	.short	21650
	.short	22674
	.short	22930
	.short	23186
	.short	23442
	.short	23698
	.short	20642
	.short	20898
	.short	21154
	.short	21410
	.short	21666
	.short	22690
	.short	22946
	.short	23202
	.short	23458
	.short	23714
	.short	20579
	.short	20835
	.short	21091
	.short	21347
	.short	21603
	.short	22627
	.short	22883
	.short	23139
	.short	23395
	.short	23651
	.short	20595
	.short	20851
	.short	21107
	.short	21363
	.short	21619
	.short	22643
	.short	22899
	.short	23155
	.short	23411
	.short	23667
	.short	20548
	.short	20804
	.short	21060
	.short	21316
	.short	21572
	.short	22596
	.short	22852
	.short	23108
	.short	23364
	.short	23620
	.short	20564
	.short	20820
	.short	21076
	.short	21332
	.short	21588
	.short	22612
	.short	22868
	.short	23124
	.short	23380
	.short	23636
	.short	20533
	.short	20789
	.short	21045
	.short	21301
	.short	21557
	.short	22581
	.short	22837
	.short	23093
	.short	23349
	.short	23605
	.short	20518
	.short	20774
	.short	21030
	.short	21286
	.short	21542
	.short	22566
	.short	22822
	.short	23078
	.short	23334
	.short	23590
	.short	20503
	.short	20759
	.short	21015
	.short	21271
	.short	21527
	.short	22551
	.short	22807
	.short	23063
	.short	23319
	.short	23575
	.short	20488
	.short	20744
	.short	21000
	.short	21256
	.short	21512
	.short	22536
	.short	22792
	.short	23048
	.short	23304
	.short	23560
	.size	_ZN3attL9ATT_ORDERE, 7596

	.type	__hip_cuid_5ba2c1623d679635,@object
